# GCN1 gather accumulate via v_fma_mix_f32 (bit-identical), sleep+s_wakeup barriers, grid-barrier poll rewrite, L1 ds_read hoist
# speedup vs baseline: 1.0223x; 1.0071x over previous
.LBB1_332:
	s_or_b64 exec, exec, s[2:3]
	s_waitcnt vmcnt(0)
	s_waitcnt vmcnt(0)
	ds_read_b128 v[58:61], v55
	ds_read_b128 v[62:65], v55 offset:1024
	ds_read_b128 v[66:69], v55 offset:2048
	ds_read_b128 v[70:73], v55 offset:3072
	ds_read_b128 v[74:77], v55 offset:4096
	ds_read_b128 v[78:81], v55 offset:5120
	ds_read_b128 v[82:85], v55 offset:6144
	ds_read_b128 v[86:89], v55 offset:7168
	ds_read_b128 v[90:93], v55 offset:8192
	ds_read_b128 v[94:97], v55 offset:9216
	s_waitcnt lgkmcnt(0)
	v_fma_mix_f32 v28, v58, 1.0, v28 op_sel_hi:[1,0,0]
	v_fma_mix_f32 v29, v58, 1.0, v29 op_sel:[1,0,0] op_sel_hi:[1,0,0]
	v_fma_mix_f32 v26, v59, 1.0, v26 op_sel_hi:[1,0,0]
	v_fma_mix_f32 v27, v59, 1.0, v27 op_sel:[1,0,0] op_sel_hi:[1,0,0]
	v_fma_mix_f32 v24, v60, 1.0, v24 op_sel_hi:[1,0,0]
	v_fma_mix_f32 v25, v60, 1.0, v25 op_sel:[1,0,0] op_sel_hi:[1,0,0]
	v_fma_mix_f32 v12, v61, 1.0, v12 op_sel_hi:[1,0,0]
	v_fma_mix_f32 v13, v61, 1.0, v13 op_sel:[1,0,0] op_sel_hi:[1,0,0]
	v_fma_mix_f32 v28, v62, 1.0, v28 op_sel_hi:[1,0,0]
	v_fma_mix_f32 v29, v62, 1.0, v29 op_sel:[1,0,0] op_sel_hi:[1,0,0]
	v_fma_mix_f32 v26, v63, 1.0, v26 op_sel_hi:[1,0,0]
	v_fma_mix_f32 v27, v63, 1.0, v27 op_sel:[1,0,0] op_sel_hi:[1,0,0]
	v_fma_mix_f32 v24, v64, 1.0, v24 op_sel_hi:[1,0,0]
	v_fma_mix_f32 v25, v64, 1.0, v25 op_sel:[1,0,0] op_sel_hi:[1,0,0]
	v_fma_mix_f32 v12, v65, 1.0, v12 op_sel_hi:[1,0,0]
	v_fma_mix_f32 v13, v65, 1.0, v13 op_sel:[1,0,0] op_sel_hi:[1,0,0]
	v_fma_mix_f32 v28, v66, 1.0, v28 op_sel_hi:[1,0,0]
	v_fma_mix_f32 v29, v66, 1.0, v29 op_sel:[1,0,0] op_sel_hi:[1,0,0]
	v_fma_mix_f32 v26, v67, 1.0, v26 op_sel_hi:[1,0,0]
	v_fma_mix_f32 v27, v67, 1.0, v27 op_sel:[1,0,0] op_sel_hi:[1,0,0]
	v_fma_mix_f32 v24, v68, 1.0, v24 op_sel_hi:[1,0,0]
	v_fma_mix_f32 v25, v68, 1.0, v25 op_sel:[1,0,0] op_sel_hi:[1,0,0]
	v_fma_mix_f32 v12, v69, 1.0, v12 op_sel_hi:[1,0,0]
	v_fma_mix_f32 v13, v69, 1.0, v13 op_sel:[1,0,0] op_sel_hi:[1,0,0]
	v_fma_mix_f32 v28, v70, 1.0, v28 op_sel_hi:[1,0,0]
	v_fma_mix_f32 v29, v70, 1.0, v29 op_sel:[1,0,0] op_sel_hi:[1,0,0]
	v_fma_mix_f32 v26, v71, 1.0, v26 op_sel_hi:[1,0,0]
	v_fma_mix_f32 v27, v71, 1.0, v27 op_sel:[1,0,0] op_sel_hi:[1,0,0]
	v_fma_mix_f32 v24, v72, 1.0, v24 op_sel_hi:[1,0,0]
	v_fma_mix_f32 v25, v72, 1.0, v25 op_sel:[1,0,0] op_sel_hi:[1,0,0]
	v_fma_mix_f32 v12, v73, 1.0, v12 op_sel_hi:[1,0,0]
	v_fma_mix_f32 v13, v73, 1.0, v13 op_sel:[1,0,0] op_sel_hi:[1,0,0]
	v_fma_mix_f32 v28, v74, 1.0, v28 op_sel_hi:[1,0,0]
	v_fma_mix_f32 v29, v74, 1.0, v29 op_sel:[1,0,0] op_sel_hi:[1,0,0]
	v_fma_mix_f32 v26, v75, 1.0, v26 op_sel_hi:[1,0,0]
	v_fma_mix_f32 v27, v75, 1.0, v27 op_sel:[1,0,0] op_sel_hi:[1,0,0]
	v_fma_mix_f32 v24, v76, 1.0, v24 op_sel_hi:[1,0,0]
	v_fma_mix_f32 v25, v76, 1.0, v25 op_sel:[1,0,0] op_sel_hi:[1,0,0]
	v_fma_mix_f32 v12, v77, 1.0, v12 op_sel_hi:[1,0,0]
	v_fma_mix_f32 v13, v77, 1.0, v13 op_sel:[1,0,0] op_sel_hi:[1,0,0]
	v_fma_mix_f32 v28, v78, 1.0, v28 op_sel_hi:[1,0,0]
	v_fma_mix_f32 v29, v78, 1.0, v29 op_sel:[1,0,0] op_sel_hi:[1,0,0]
	v_fma_mix_f32 v26, v79, 1.0, v26 op_sel_hi:[1,0,0]
	v_fma_mix_f32 v27, v79, 1.0, v27 op_sel:[1,0,0] op_sel_hi:[1,0,0]
	v_fma_mix_f32 v24, v80, 1.0, v24 op_sel_hi:[1,0,0]
	v_fma_mix_f32 v25, v80, 1.0, v25 op_sel:[1,0,0] op_sel_hi:[1,0,0]
	v_fma_mix_f32 v12, v81, 1.0, v12 op_sel_hi:[1,0,0]
	v_fma_mix_f32 v13, v81, 1.0, v13 op_sel:[1,0,0] op_sel_hi:[1,0,0]
	v_fma_mix_f32 v28, v82, 1.0, v28 op_sel_hi:[1,0,0]
	v_fma_mix_f32 v29, v82, 1.0, v29 op_sel:[1,0,0] op_sel_hi:[1,0,0]
	v_fma_mix_f32 v26, v83, 1.0, v26 op_sel_hi:[1,0,0]
	v_fma_mix_f32 v27, v83, 1.0, v27 op_sel:[1,0,0] op_sel_hi:[1,0,0]
	v_fma_mix_f32 v24, v84, 1.0, v24 op_sel_hi:[1,0,0]
	v_fma_mix_f32 v25, v84, 1.0, v25 op_sel:[1,0,0] op_sel_hi:[1,0,0]
	v_fma_mix_f32 v12, v85, 1.0, v12 op_sel_hi:[1,0,0]
	v_fma_mix_f32 v13, v85, 1.0, v13 op_sel:[1,0,0] op_sel_hi:[1,0,0]
	v_fma_mix_f32 v28, v86, 1.0, v28 op_sel_hi:[1,0,0]
	v_fma_mix_f32 v29, v86, 1.0, v29 op_sel:[1,0,0] op_sel_hi:[1,0,0]
	v_fma_mix_f32 v26, v87, 1.0, v26 op_sel_hi:[1,0,0]
	v_fma_mix_f32 v27, v87, 1.0, v27 op_sel:[1,0,0] op_sel_hi:[1,0,0]
	v_fma_mix_f32 v24, v88, 1.0, v24 op_sel_hi:[1,0,0]
	v_fma_mix_f32 v25, v88, 1.0, v25 op_sel:[1,0,0] op_sel_hi:[1,0,0]
	v_fma_mix_f32 v12, v89, 1.0, v12 op_sel_hi:[1,0,0]
	v_fma_mix_f32 v13, v89, 1.0, v13 op_sel:[1,0,0] op_sel_hi:[1,0,0]
	v_fma_mix_f32 v28, v90, 1.0, v28 op_sel_hi:[1,0,0]
	v_fma_mix_f32 v29, v90, 1.0, v29 op_sel:[1,0,0] op_sel_hi:[1,0,0]
	v_fma_mix_f32 v26, v91, 1.0, v26 op_sel_hi:[1,0,0]
	v_fma_mix_f32 v27, v91, 1.0, v27 op_sel:[1,0,0] op_sel_hi:[1,0,0]
	v_fma_mix_f32 v24, v92, 1.0, v24 op_sel_hi:[1,0,0]
	v_fma_mix_f32 v25, v92, 1.0, v25 op_sel:[1,0,0] op_sel_hi:[1,0,0]
	v_fma_mix_f32 v12, v93, 1.0, v12 op_sel_hi:[1,0,0]
	v_fma_mix_f32 v13, v93, 1.0, v13 op_sel:[1,0,0] op_sel_hi:[1,0,0]
	v_fma_mix_f32 v28, v94, 1.0, v28 op_sel_hi:[1,0,0]
	v_fma_mix_f32 v29, v94, 1.0, v29 op_sel:[1,0,0] op_sel_hi:[1,0,0]
	v_fma_mix_f32 v26, v95, 1.0, v26 op_sel_hi:[1,0,0]
	v_fma_mix_f32 v27, v95, 1.0, v27 op_sel:[1,0,0] op_sel_hi:[1,0,0]
	v_fma_mix_f32 v24, v96, 1.0, v24 op_sel_hi:[1,0,0]
	v_fma_mix_f32 v25, v96, 1.0, v25 op_sel:[1,0,0] op_sel_hi:[1,0,0]
	v_fma_mix_f32 v12, v97, 1.0, v12 op_sel_hi:[1,0,0]
	v_fma_mix_f32 v13, v97, 1.0, v13 op_sel:[1,0,0] op_sel_hi:[1,0,0]
	s_waitcnt lgkmcnt(0)
	s_add_i32 s18, s18, 10
	s_cmp_ge_i32 s19, s17
	s_cbranch_scc1 .LBB1_309
